# loop-edge edits: band tile loop and indexer step-1 loop control reduced to one compare/select plus one conditional back-edge (drops 6-8 SALU and 2 branches per iteration)
# baseline (speedup 1.0000x reference)
.LBB0_380:
	s_add_i32 s79, s0, 8
	s_cmp_gt_i32 s79, s81
	s_cselect_b64 s[18:19], -1, 0
	s_cbranch_scc1 .LBB0_382
	v_mad_i64_i32 v[4:5], s[58:59], s95, v240, v[220:221]
	global_load_dwordx4 v[68:71], v[4:5], off offset:3328
	global_load_dwordx4 v[64:67], v[4:5], off offset:3360
	global_load_dwordx4 v[60:63], v[4:5], off offset:3392
	global_load_dwordx4 v[56:59], v[4:5], off offset:3424

.Lidx_join:
	v_permlane32_swap_b32_e32 v4, v6
	v_permlane32_swap_b32_e32 v5, v7
	v_permlane32_swap_b32_e32 v8, v10
	v_permlane32_swap_b32_e32 v9, v11
	s_and_b64 vcc, exec, s[18:19]
	global_store_dwordx4 v231, v[4:7], s[12:13]
	global_store_dwordx4 v231, v[8:11], s[12:13] offset:16
	v_add_u32_e32 v231, 0x4000, v231
	s_addk_i32 s95, 0x100
	s_cbranch_vccnz .LBB0_390
	s_waitcnt vmcnt(2)
	v_mov_b64_e32 v[52:53], v[56:57]
	v_mov_b64_e32 v[74:75], v[62:63]
	v_mov_b64_e32 v[78:79], v[66:67]
	v_mov_b64_e32 v[82:83], v[70:71]
	v_mov_b64_e32 v[54:55], v[58:59]
	v_mov_b64_e32 v[72:73], v[60:61]
	v_mov_b64_e32 v[76:77], v[64:65]
	v_mov_b64_e32 v[80:81], v[68:69]
	s_mov_b32 s0, s79
	s_branch .LBB0_380

.LBB0_1259:
	s_cmp_le_u32 s41, s51
	s_cselect_b64 s[60:61], -1, 0
	s_cbranch_scc0 .LBB0_1265
	s_andn2_b64 vcc, exec, s[52:53]
	s_cbranch_vccnz .LBB0_1265
	global_load_dwordx4 v[84:87], v[160:161], off
	global_load_dwordx4 v[88:91], v[160:161], off offset:32
	global_load_dwordx4 v[92:95], v[160:161], off offset:64
	global_load_dwordx4 v[96:99], v[160:161], off offset:96
	global_load_dwordx4 v[4:7], v[162:163], off
	global_load_dwordx4 v[8:11], v[162:163], off offset:32
	global_load_dwordx4 v[12:15], v[162:163], off offset:64
	global_load_dwordx4 v[16:19], v[162:163], off offset:96
	global_load_dwordx4 v[68:71], v[164:165], off
	global_load_dwordx4 v[72:75], v[166:167], off
	global_load_dwordx4 v[76:79], v[168:169], off
	global_load_dwordx4 v[80:83], v[170:171], off
.LBB0_1265:
	s_waitcnt vmcnt(0)
	v_mfma_f32_32x32x16_bf16 v[52:67], v[144:147], v[124:127], 0
	ds_write_b128 v191, v[128:131] offset:32768
	ds_write_b128 v191, v[120:123] offset:33280
	ds_write_b128 v191, v[104:107] offset:33792
	ds_write_b128 v191, v[100:103] offset:34304
	ds_read2_b32 v[198:199], v153 offset0:26 offset1:27
	s_and_b64 vcc, exec, s[60:61]
	v_mfma_f32_32x32x16_bf16 v[52:67], v[140:143], v[116:119], v[52:67]
	v_mfma_f32_32x32x16_bf16 v[52:67], v[136:139], v[112:115], v[52:67]
	v_mfma_f32_32x32x16_bf16 v[52:67], v[132:135], v[108:111], v[52:67]
	s_cbranch_vccnz .Lband_nopf
	global_load_dwordx4 v[144:147], v[180:181], off
	global_load_dwordx4 v[140:143], v[180:181], off offset:32
	global_load_dwordx4 v[136:139], v[180:181], off offset:64
	global_load_dwordx4 v[132:135], v[180:181], off offset:96
	global_load_dwordx4 v[128:131], v[178:179], off
	global_load_dwordx4 v[120:123], v[176:177], off
	global_load_dwordx4 v[104:107], v[174:175], off
	global_load_dwordx4 v[100:103], v[172:173], off

.LBB0_1267:
	v_add_f32_e32 v197, v57, v58
	v_fmac_f32_e32 v197, v194, v56
	s_add_i32 s41, s41, -1
	v_lshl_add_u64 v[172:173], v[172:173], 0, v[206:207]
	v_lshl_add_u64 v[174:175], v[174:175], 0, v[206:207]
	v_lshl_add_u64 v[176:177], v[176:177], 0, v[206:207]
	v_lshl_add_u64 v[178:179], v[178:179], 0, v[206:207]
	v_lshl_add_u64 v[180:181], v[180:181], 0, v[206:207]
	v_add_u32_e32 v153, 0x80, v153
	v_mov_b32_e32 v196, v195
	v_mov_b32_e32 v194, v197
	s_and_b64 vcc, exec, s[60:61]
	s_cbranch_vccz .LBB0_1259
